# MoE k-loop back-edge rotation: counters, pointer bumps, stage offsets and DMA m0 bases computed before the post-burst barrier; parity selects folded; m0 save/restore dropped
# speedup vs baseline: 1.0175x; 1.0175x over previous
.LBB0_1173:
	v_bfe_u32 v5, v3, 2, 2
	v_and_b32_e32 v22, 12, v3
	v_lshrrev_b32_e32 v4, 4, v3
	v_lshrrev_b32_e64 v22, v22, s90
	v_lshlrev_b32_e32 v23, 8, v3
	v_lshlrev_b32_e32 v24, 9, v5
	s_movk_i32 s8, 0x3000
	v_xor_b32_e32 v4, v22, v4
	v_lshrrev_b32_e32 v22, 2, v3
	v_and_or_b32 v23, v23, s8, v24
	s_lshl_b32 s8, s5, 2
	v_and_b32_e32 v1, 15, v3
	v_and_b32_e32 v22, 4, v22
	s_and_b32 s8, s8, 12
	v_or_b32_e32 v1, s2, v1
	v_lshlrev_b32_e32 v4, 4, v4
	v_bitop3_b32 v5, v22, s8, v5 bitop3:0x36
	v_lshlrev_b32_e32 v3, 3, v3
	v_lshl_or_b32 v5, v5, 5, v23
	v_and_b32_e32 v3, 24, v3
	s_lshl_b32 s33, s5, 10
	v_lshlrev_b32_e32 v1, 6, v1
	v_and_b32_e32 v4, 48, v4
	s_movk_i32 s8, 0x60
	v_or_b32_e32 v214, v5, v3
	s_add_i32 s33, s33, 0
	v_add3_u32 v213, 0, v1, v4
	v_bitop3_b32 v217, v5, 32, v3 bitop3:0x36
	v_bitop3_b32 v216, v5, 64, v3 bitop3:0x36
	v_bitop3_b32 v215, v5, s8, v3 bitop3:0x36
	v_mov_b32_e32 v4, v2
	v_mov_b32_e32 v5, v2
	s_cmp_gt_i32 s34, 0
	s_mov_b64 s[8:9], 0xc0000
	v_mov_b32_e32 v3, v2
	v_mov_b64_e32 v[108:109], v[4:5]
	v_mov_b64_e32 v[116:117], v[4:5]
	v_mov_b64_e32 v[120:121], v[4:5]
	v_mov_b64_e32 v[128:129], v[4:5]
	v_mov_b64_e32 v[124:125], v[4:5]
	v_mov_b64_e32 v[132:133], v[4:5]
	v_mov_b64_e32 v[136:137], v[4:5]
	v_mov_b64_e32 v[140:141], v[4:5]
	v_mov_b64_e32 v[144:145], v[4:5]
	v_mov_b64_e32 v[148:149], v[4:5]
	v_mov_b64_e32 v[112:113], v[4:5]
	v_mov_b64_e32 v[104:105], v[4:5]
	v_mov_b64_e32 v[100:101], v[4:5]
	v_mov_b64_e32 v[92:93], v[4:5]
	v_mov_b64_e32 v[96:97], v[4:5]
	v_mov_b64_e32 v[88:89], v[4:5]
	v_mov_b64_e32 v[84:85], v[4:5]
	v_mov_b64_e32 v[76:77], v[4:5]
	v_mov_b64_e32 v[80:81], v[4:5]
	v_mov_b64_e32 v[72:73], v[4:5]
	v_mov_b64_e32 v[68:69], v[4:5]
	v_mov_b64_e32 v[60:61], v[4:5]
	v_mov_b64_e32 v[64:65], v[4:5]
	v_mov_b64_e32 v[56:57], v[4:5]
	v_mov_b64_e32 v[52:53], v[4:5]
	v_mov_b64_e32 v[44:45], v[4:5]
	v_mov_b64_e32 v[48:49], v[4:5]
	v_mov_b64_e32 v[40:41], v[4:5]
	v_mov_b64_e32 v[36:37], v[4:5]
	v_mov_b64_e32 v[28:29], v[4:5]
	v_mov_b64_e32 v[32:33], v[4:5]
	v_mov_b64_e32 v[24:25], v[4:5]
	s_mov_b32 s2, 2
	s_mov_b32 s5, 0
	s_cselect_b64 s[76:77], -1, 0
	v_lshl_add_u64 v[204:205], v[200:201], 0, s[70:71]
	v_lshl_add_u64 v[206:207], v[198:199], 0, s[70:71]
	v_lshl_add_u64 v[208:209], v[202:203], 0, s[8:9]
	v_mov_b64_e32 v[106:107], v[2:3]
	v_mov_b64_e32 v[114:115], v[2:3]
	v_mov_b64_e32 v[118:119], v[2:3]
	v_mov_b64_e32 v[126:127], v[2:3]
	v_mov_b64_e32 v[122:123], v[2:3]
	v_mov_b64_e32 v[130:131], v[2:3]
	v_mov_b64_e32 v[134:135], v[2:3]
	v_mov_b64_e32 v[138:139], v[2:3]
	v_mov_b64_e32 v[142:143], v[2:3]
	v_mov_b64_e32 v[146:147], v[2:3]
	v_mov_b64_e32 v[110:111], v[2:3]
	v_mov_b64_e32 v[102:103], v[2:3]
	v_mov_b64_e32 v[98:99], v[2:3]
	v_mov_b64_e32 v[90:91], v[2:3]
	v_mov_b64_e32 v[94:95], v[2:3]
	v_mov_b64_e32 v[86:87], v[2:3]
	v_mov_b64_e32 v[82:83], v[2:3]
	v_mov_b64_e32 v[74:75], v[2:3]
	v_mov_b64_e32 v[78:79], v[2:3]
	v_mov_b64_e32 v[70:71], v[2:3]
	v_mov_b64_e32 v[66:67], v[2:3]
	v_mov_b64_e32 v[58:59], v[2:3]
	v_mov_b64_e32 v[62:63], v[2:3]
	v_mov_b64_e32 v[54:55], v[2:3]
	v_mov_b64_e32 v[50:51], v[2:3]
	v_mov_b64_e32 v[42:43], v[2:3]
	v_mov_b64_e32 v[46:47], v[2:3]
	v_mov_b64_e32 v[38:39], v[2:3]
	v_mov_b64_e32 v[34:35], v[2:3]
	v_mov_b64_e32 v[26:27], v[2:3]
	v_mov_b64_e32 v[30:31], v[2:3]
	v_mov_b64_e32 v[22:23], v[2:3]
	s_mov_b32 s34, 0
	v_add_u32_e32 v240, 0x10000, v214
	v_add_u32_e32 v241, 0x10000, v217
	v_add_u32_e32 v242, 0x10000, v216
	v_add_u32_e32 v243, 0x10000, v215
	s_mov_b32 s98, 0
	s_add_i32 s99, s33, 0x8000
	s_add_i32 s100, s33, 0x17fc0
	s_branch .LBB0_1175
.LBB0_1174:
	s_setprio 0
	s_add_i32 s34, s34, 1
	s_add_i32 s5, s5, 1
	s_and_b32 s5, s5, 3
	s_lshl_b32 s98, s5, 14
	s_cmp_eq_u32 s5, 3
	s_cselect_b32 s98, 0x18000, s98
	s_cmp_eq_u32 s5, 0
	s_cselect_b32 s99, 0x8000, 0
	s_cselect_b32 s100, 0x14000, 0
	s_add_i32 s99, s99, s33
	s_add_i32 s100, s100, s33
	s_addk_i32 s100, 0x3fc0
	v_lshl_add_u64 v[204:205], v[204:205], 0, 64
	v_lshl_add_u64 v[206:207], v[206:207], 0, 64
	v_lshl_add_u64 v[208:209], v[208:209], 0, s[66:67]
	s_waitcnt lgkmcnt(0)
	s_barrier
.LBB0_1175:
	s_waitcnt lgkmcnt(14)
	ds_read_b64_tr_b16 v[150:151], v214 offset:49152
	ds_read_b64_tr_b16 v[152:153], v214 offset:51200
	ds_read_b64_tr_b16 v[154:155], v217 offset:49152
	ds_read_b64_tr_b16 v[156:157], v217 offset:51200
	s_waitcnt lgkmcnt(14)
	ds_read_b64_tr_b16 v[158:159], v216 offset:49152
	ds_read_b64_tr_b16 v[160:161], v216 offset:51200
	ds_read_b64_tr_b16 v[162:163], v215 offset:49152
	ds_read_b64_tr_b16 v[164:165], v215 offset:51200
	v_add_u32_e32 v1, s98, v213
	s_waitcnt lgkmcnt(14)
	ds_read_b128 v[194:197], v1
	ds_read_b128 v[190:193], v1 offset:1024
	ds_read_b128 v[186:189], v1 offset:2048
	ds_read_b128 v[182:185], v1 offset:3072
	s_waitcnt lgkmcnt(14)
	ds_read_b128 v[178:181], v1 offset:4096
	ds_read_b128 v[174:177], v1 offset:5120
	ds_read_b128 v[170:173], v1 offset:6144
	ds_read_b128 v[166:169], v1 offset:7168
	s_mov_b32 m0, s99
	s_add_i32 s8, s99, 0x2000
	global_load_lds_dwordx4 v[206:207], off
	s_mov_b32 m0, s8
	s_add_i32 s8, s100, 0x2000
	global_load_lds_dwordx4 v[204:205], off
	s_mov_b32 m0, s100
	s_nop 0
	global_load_lds_dwordx4 v[206:207], off offset:64
	s_mov_b32 m0, s8
	s_nop 0
	global_load_lds_dwordx4 v[204:205], off offset:64
	v_add_u32_e32 v1, 0x10000, v218
	s_waitcnt vmcnt(8)
	v_cvt_pk_bf16_f32 v224, v224, v225
	v_cvt_pk_bf16_f32 v225, v226, v227
	v_cvt_pk_bf16_f32 v226, v228, v229
	v_cvt_pk_bf16_f32 v227, v230, v231
	ds_write_b128 v1, v[224:227]
	v_cvt_pk_bf16_f32 v232, v232, v233
	v_cvt_pk_bf16_f32 v233, v234, v235
	v_cvt_pk_bf16_f32 v234, v236, v237
	v_cvt_pk_bf16_f32 v235, v238, v239
	ds_write_b128 v1, v[232:235] offset:8192
	global_load_dwordx4 v[224:227], v[208:209], off
	global_load_dwordx4 v[228:231], v[208:209], off offset:16
	v_lshl_add_u64 v[4:5], v[208:209], 0, s[62:63]
	global_load_dwordx4 v[232:235], v[4:5], off
	global_load_dwordx4 v[236:239], v[4:5], off offset:16
	s_waitcnt lgkmcnt(0)
	s_barrier
	s_setprio 1
	v_cndmask_b32_e64 v1, 0, 1, s[76:77]
	v_cmp_ne_u32_e64 s[8:9], 1, v1
	s_andn2_b64 vcc, exec, s[76:77]
	s_cbranch_vccnz .Lmoe_end_even
	s_waitcnt lgkmcnt(9)
	v_mfma_f32_16x16x32_bf16 v[146:149], v[150:153], v[194:197], v[146:149]
	v_mfma_f32_16x16x32_bf16 v[142:145], v[154:157], v[194:197], v[142:145]
	v_mfma_f32_16x16x32_bf16 v[138:141], v[158:161], v[194:197], v[138:141]
	v_mfma_f32_16x16x32_bf16 v[134:137], v[162:165], v[194:197], v[134:137]
	s_waitcnt lgkmcnt(8)
	v_mfma_f32_16x16x32_bf16 v[130:133], v[150:153], v[190:193], v[130:133]
	v_mfma_f32_16x16x32_bf16 v[122:125], v[154:157], v[190:193], v[122:125]
	v_mfma_f32_16x16x32_bf16 v[126:129], v[158:161], v[190:193], v[126:129]
	v_mfma_f32_16x16x32_bf16 v[118:121], v[162:165], v[190:193], v[118:121]
	s_waitcnt lgkmcnt(7)
	v_mfma_f32_16x16x32_bf16 v[114:117], v[150:153], v[186:189], v[114:117]
	v_mfma_f32_16x16x32_bf16 v[106:109], v[154:157], v[186:189], v[106:109]
	v_mfma_f32_16x16x32_bf16 v[110:113], v[158:161], v[186:189], v[110:113]
	v_mfma_f32_16x16x32_bf16 v[102:105], v[162:165], v[186:189], v[102:105]
	s_waitcnt lgkmcnt(6)
	v_mfma_f32_16x16x32_bf16 v[98:101], v[150:153], v[182:185], v[98:101]
	v_mfma_f32_16x16x32_bf16 v[90:93], v[154:157], v[182:185], v[90:93]
	v_mfma_f32_16x16x32_bf16 v[94:97], v[158:161], v[182:185], v[94:97]
	v_mfma_f32_16x16x32_bf16 v[86:89], v[162:165], v[182:185], v[86:89]
	s_waitcnt lgkmcnt(5)
	v_mfma_f32_16x16x32_bf16 v[82:85], v[150:153], v[178:181], v[82:85]
	v_mfma_f32_16x16x32_bf16 v[74:77], v[154:157], v[178:181], v[74:77]
	v_mfma_f32_16x16x32_bf16 v[78:81], v[158:161], v[178:181], v[78:81]
	v_mfma_f32_16x16x32_bf16 v[70:73], v[162:165], v[178:181], v[70:73]
	s_waitcnt lgkmcnt(4)
	v_mfma_f32_16x16x32_bf16 v[66:69], v[150:153], v[174:177], v[66:69]
	v_mfma_f32_16x16x32_bf16 v[58:61], v[154:157], v[174:177], v[58:61]
	v_mfma_f32_16x16x32_bf16 v[62:65], v[158:161], v[174:177], v[62:65]
	v_mfma_f32_16x16x32_bf16 v[54:57], v[162:165], v[174:177], v[54:57]
	s_waitcnt lgkmcnt(3)
	v_mfma_f32_16x16x32_bf16 v[50:53], v[150:153], v[170:173], v[50:53]
	v_mfma_f32_16x16x32_bf16 v[42:45], v[154:157], v[170:173], v[42:45]
	v_mfma_f32_16x16x32_bf16 v[46:49], v[158:161], v[170:173], v[46:49]
	v_mfma_f32_16x16x32_bf16 v[38:41], v[162:165], v[170:173], v[38:41]
	s_waitcnt lgkmcnt(2)
	v_mfma_f32_16x16x32_bf16 v[34:37], v[150:153], v[166:169], v[34:37]
	v_mfma_f32_16x16x32_bf16 v[26:29], v[154:157], v[166:169], v[26:29]
	v_mfma_f32_16x16x32_bf16 v[30:33], v[158:161], v[166:169], v[30:33]
	v_mfma_f32_16x16x32_bf16 v[22:25], v[162:165], v[166:169], v[22:25]
.Lmoe_end_even:
	s_setprio 0
	s_add_i32 s34, s34, 1
	s_add_i32 s5, s5, 1
	s_and_b32 s5, s5, 3
	s_lshl_b32 s98, s5, 14
	s_cmp_eq_u32 s5, 3
	s_cselect_b32 s98, 0x18000, s98
	v_lshl_add_u64 v[204:205], v[204:205], 0, 64
	v_lshl_add_u64 v[206:207], v[206:207], 0, 64
	v_lshl_add_u64 v[208:209], v[208:209], 0, s[66:67]
	s_cmp_eq_u32 s34, 61
	s_waitcnt lgkmcnt(0)
	s_barrier
	s_cbranch_scc1 .Lmoe_t61
	s_waitcnt lgkmcnt(14)
	ds_read_b64_tr_b16 v[150:151], v240
	ds_read_b64_tr_b16 v[152:153], v240 offset:2048
	ds_read_b64_tr_b16 v[154:155], v241
	ds_read_b64_tr_b16 v[156:157], v241 offset:2048
	s_waitcnt lgkmcnt(14)
	ds_read_b64_tr_b16 v[158:159], v242
	ds_read_b64_tr_b16 v[160:161], v242 offset:2048
	ds_read_b64_tr_b16 v[162:163], v243
	ds_read_b64_tr_b16 v[164:165], v243 offset:2048
	v_add_u32_e32 v1, s98, v213
	s_waitcnt lgkmcnt(14)
	ds_read_b128 v[194:197], v1
	ds_read_b128 v[190:193], v1 offset:1024
	ds_read_b128 v[186:189], v1 offset:2048
	ds_read_b128 v[182:185], v1 offset:3072
	s_waitcnt lgkmcnt(14)
	ds_read_b128 v[178:181], v1 offset:4096
	ds_read_b128 v[174:177], v1 offset:5120
	ds_read_b128 v[170:173], v1 offset:6144
	ds_read_b128 v[166:169], v1 offset:7168
	v_add_u32_e32 v1, 0xc000, v218
	s_waitcnt vmcnt(6)
	v_cvt_pk_bf16_f32 v18, v18, v19
	v_cvt_pk_bf16_f32 v19, v20, v21
	v_cvt_pk_bf16_f32 v20, v14, v15
	v_cvt_pk_bf16_f32 v21, v16, v17
	ds_write_b128 v1, v[18:21]
	v_cvt_pk_bf16_f32 v4, v10, v11
	v_cvt_pk_bf16_f32 v5, v12, v13
	v_cvt_pk_bf16_f32 v6, v6, v7
	v_cvt_pk_bf16_f32 v7, v8, v9
	ds_write_b128 v1, v[4:7] offset:8192
	global_load_dwordx4 v[18:21], v[208:209], off
	global_load_dwordx4 v[14:17], v[208:209], off offset:16
	v_lshl_add_u64 v[4:5], v[208:209], 0, s[62:63]
	global_load_dwordx4 v[10:13], v[4:5], off
	global_load_dwordx4 v[6:9], v[4:5], off offset:16
	s_waitcnt lgkmcnt(0)
	s_barrier
	s_setprio 1
	v_cndmask_b32_e64 v1, 0, 1, s[76:77]
	v_cmp_ne_u32_e64 s[8:9], 1, v1
	s_andn2_b64 vcc, exec, s[76:77]
	s_cbranch_vccnz .LBB0_1174
	s_waitcnt lgkmcnt(9)
	v_mfma_f32_16x16x32_bf16 v[146:149], v[150:153], v[194:197], v[146:149]
	v_mfma_f32_16x16x32_bf16 v[142:145], v[154:157], v[194:197], v[142:145]
	v_mfma_f32_16x16x32_bf16 v[138:141], v[158:161], v[194:197], v[138:141]
	v_mfma_f32_16x16x32_bf16 v[134:137], v[162:165], v[194:197], v[134:137]
	s_waitcnt lgkmcnt(8)
	v_mfma_f32_16x16x32_bf16 v[130:133], v[150:153], v[190:193], v[130:133]
	v_mfma_f32_16x16x32_bf16 v[122:125], v[154:157], v[190:193], v[122:125]
	v_mfma_f32_16x16x32_bf16 v[126:129], v[158:161], v[190:193], v[126:129]
	v_mfma_f32_16x16x32_bf16 v[118:121], v[162:165], v[190:193], v[118:121]
	s_waitcnt lgkmcnt(7)
	v_mfma_f32_16x16x32_bf16 v[114:117], v[150:153], v[186:189], v[114:117]
	v_mfma_f32_16x16x32_bf16 v[106:109], v[154:157], v[186:189], v[106:109]
	v_mfma_f32_16x16x32_bf16 v[110:113], v[158:161], v[186:189], v[110:113]
	v_mfma_f32_16x16x32_bf16 v[102:105], v[162:165], v[186:189], v[102:105]
	s_waitcnt lgkmcnt(6)
	v_mfma_f32_16x16x32_bf16 v[98:101], v[150:153], v[182:185], v[98:101]
	v_mfma_f32_16x16x32_bf16 v[90:93], v[154:157], v[182:185], v[90:93]
	v_mfma_f32_16x16x32_bf16 v[94:97], v[158:161], v[182:185], v[94:97]
	v_mfma_f32_16x16x32_bf16 v[86:89], v[162:165], v[182:185], v[86:89]
	s_waitcnt lgkmcnt(5)
	v_mfma_f32_16x16x32_bf16 v[82:85], v[150:153], v[178:181], v[82:85]
	v_mfma_f32_16x16x32_bf16 v[74:77], v[154:157], v[178:181], v[74:77]
	v_mfma_f32_16x16x32_bf16 v[78:81], v[158:161], v[178:181], v[78:81]
	v_mfma_f32_16x16x32_bf16 v[70:73], v[162:165], v[178:181], v[70:73]
	s_waitcnt lgkmcnt(4)
	v_mfma_f32_16x16x32_bf16 v[66:69], v[150:153], v[174:177], v[66:69]
	v_mfma_f32_16x16x32_bf16 v[58:61], v[154:157], v[174:177], v[58:61]
	v_mfma_f32_16x16x32_bf16 v[62:65], v[158:161], v[174:177], v[62:65]
	v_mfma_f32_16x16x32_bf16 v[54:57], v[162:165], v[174:177], v[54:57]
	s_waitcnt lgkmcnt(3)
	v_mfma_f32_16x16x32_bf16 v[50:53], v[150:153], v[170:173], v[50:53]
	v_mfma_f32_16x16x32_bf16 v[42:45], v[154:157], v[170:173], v[42:45]
	v_mfma_f32_16x16x32_bf16 v[46:49], v[158:161], v[170:173], v[46:49]
	v_mfma_f32_16x16x32_bf16 v[38:41], v[162:165], v[170:173], v[38:41]
	s_waitcnt lgkmcnt(2)
	v_mfma_f32_16x16x32_bf16 v[34:37], v[150:153], v[166:169], v[34:37]
	v_mfma_f32_16x16x32_bf16 v[26:29], v[154:157], v[166:169], v[26:29]
	v_mfma_f32_16x16x32_bf16 v[30:33], v[158:161], v[166:169], v[30:33]
	v_mfma_f32_16x16x32_bf16 v[22:25], v[162:165], v[166:169], v[22:25]
	s_branch .LBB0_1174
.Lmoe_t61:
	s_waitcnt lgkmcnt(14)
	ds_read_b64_tr_b16 v[150:151], v240
	ds_read_b64_tr_b16 v[152:153], v240 offset:2048
	ds_read_b64_tr_b16 v[154:155], v241
	ds_read_b64_tr_b16 v[156:157], v241 offset:2048
	s_waitcnt lgkmcnt(14)
	ds_read_b64_tr_b16 v[158:159], v242
	ds_read_b64_tr_b16 v[160:161], v242 offset:2048
	ds_read_b64_tr_b16 v[162:163], v243
	ds_read_b64_tr_b16 v[164:165], v243 offset:2048
	v_add_u32_e32 v1, s98, v213
	s_waitcnt lgkmcnt(14)
	ds_read_b128 v[194:197], v1
	ds_read_b128 v[190:193], v1 offset:1024
	ds_read_b128 v[186:189], v1 offset:2048
	ds_read_b128 v[182:185], v1 offset:3072
	s_waitcnt lgkmcnt(14)
	ds_read_b128 v[178:181], v1 offset:4096
	ds_read_b128 v[174:177], v1 offset:5120
	ds_read_b128 v[170:173], v1 offset:6144
	ds_read_b128 v[166:169], v1 offset:7168
	v_add_u32_e32 v1, 0xc000, v218
	s_waitcnt vmcnt(6)
	v_cvt_pk_bf16_f32 v18, v18, v19
	v_cvt_pk_bf16_f32 v19, v20, v21
	v_cvt_pk_bf16_f32 v20, v14, v15
	v_cvt_pk_bf16_f32 v21, v16, v17
	ds_write_b128 v1, v[18:21]
	v_cvt_pk_bf16_f32 v4, v10, v11
	v_cvt_pk_bf16_f32 v5, v12, v13
	v_cvt_pk_bf16_f32 v6, v6, v7
	v_cvt_pk_bf16_f32 v7, v8, v9
	ds_write_b128 v1, v[4:7] offset:8192
	s_waitcnt lgkmcnt(0)
	s_barrier
	s_setprio 1
	v_cndmask_b32_e64 v1, 0, 1, s[76:77]
	v_cmp_ne_u32_e64 s[8:9], 1, v1
	s_andn2_b64 vcc, exec, s[76:77]
	s_cbranch_vccnz .Lmoe_end_t61
	s_waitcnt lgkmcnt(9)
	v_mfma_f32_16x16x32_bf16 v[146:149], v[150:153], v[194:197], v[146:149]
	v_mfma_f32_16x16x32_bf16 v[142:145], v[154:157], v[194:197], v[142:145]
	v_mfma_f32_16x16x32_bf16 v[138:141], v[158:161], v[194:197], v[138:141]
	v_mfma_f32_16x16x32_bf16 v[134:137], v[162:165], v[194:197], v[134:137]
	s_waitcnt lgkmcnt(8)
	v_mfma_f32_16x16x32_bf16 v[130:133], v[150:153], v[190:193], v[130:133]
	v_mfma_f32_16x16x32_bf16 v[122:125], v[154:157], v[190:193], v[122:125]
	v_mfma_f32_16x16x32_bf16 v[126:129], v[158:161], v[190:193], v[126:129]
	v_mfma_f32_16x16x32_bf16 v[118:121], v[162:165], v[190:193], v[118:121]
	s_waitcnt lgkmcnt(7)
	v_mfma_f32_16x16x32_bf16 v[114:117], v[150:153], v[186:189], v[114:117]
	v_mfma_f32_16x16x32_bf16 v[106:109], v[154:157], v[186:189], v[106:109]
	v_mfma_f32_16x16x32_bf16 v[110:113], v[158:161], v[186:189], v[110:113]
	v_mfma_f32_16x16x32_bf16 v[102:105], v[162:165], v[186:189], v[102:105]
	s_waitcnt lgkmcnt(6)
	v_mfma_f32_16x16x32_bf16 v[98:101], v[150:153], v[182:185], v[98:101]
	v_mfma_f32_16x16x32_bf16 v[90:93], v[154:157], v[182:185], v[90:93]
	v_mfma_f32_16x16x32_bf16 v[94:97], v[158:161], v[182:185], v[94:97]
	v_mfma_f32_16x16x32_bf16 v[86:89], v[162:165], v[182:185], v[86:89]
	s_waitcnt lgkmcnt(5)
	v_mfma_f32_16x16x32_bf16 v[82:85], v[150:153], v[178:181], v[82:85]
	v_mfma_f32_16x16x32_bf16 v[74:77], v[154:157], v[178:181], v[74:77]
	v_mfma_f32_16x16x32_bf16 v[78:81], v[158:161], v[178:181], v[78:81]
	v_mfma_f32_16x16x32_bf16 v[70:73], v[162:165], v[178:181], v[70:73]
	s_waitcnt lgkmcnt(4)
	v_mfma_f32_16x16x32_bf16 v[66:69], v[150:153], v[174:177], v[66:69]
	v_mfma_f32_16x16x32_bf16 v[58:61], v[154:157], v[174:177], v[58:61]
	v_mfma_f32_16x16x32_bf16 v[62:65], v[158:161], v[174:177], v[62:65]
	v_mfma_f32_16x16x32_bf16 v[54:57], v[162:165], v[174:177], v[54:57]
	s_waitcnt lgkmcnt(3)
	v_mfma_f32_16x16x32_bf16 v[50:53], v[150:153], v[170:173], v[50:53]
	v_mfma_f32_16x16x32_bf16 v[42:45], v[154:157], v[170:173], v[42:45]
	v_mfma_f32_16x16x32_bf16 v[46:49], v[158:161], v[170:173], v[46:49]
	v_mfma_f32_16x16x32_bf16 v[38:41], v[162:165], v[170:173], v[38:41]
	s_waitcnt lgkmcnt(2)
	v_mfma_f32_16x16x32_bf16 v[34:37], v[150:153], v[166:169], v[34:37]
	v_mfma_f32_16x16x32_bf16 v[26:29], v[154:157], v[166:169], v[26:29]
	v_mfma_f32_16x16x32_bf16 v[30:33], v[158:161], v[166:169], v[30:33]
	v_mfma_f32_16x16x32_bf16 v[22:25], v[162:165], v[166:169], v[22:25]
.Lmoe_end_t61:
	s_setprio 0
	s_add_i32 s34, s34, 1
	s_add_i32 s5, s5, 1
	s_and_b32 s5, s5, 3
	s_waitcnt lgkmcnt(0)
	s_barrier

	.amdhsa_kernel _Z10fwd_kernel6Params
		.amdhsa_group_segment_fixed_size 0
		.amdhsa_private_segment_fixed_size 0
		.amdhsa_kernarg_size 528
		.amdhsa_user_sgpr_count 2
		.amdhsa_user_sgpr_dispatch_ptr 0
		.amdhsa_user_sgpr_queue_ptr 0
		.amdhsa_user_sgpr_kernarg_segment_ptr 1
		.amdhsa_user_sgpr_dispatch_id 0
		.amdhsa_user_sgpr_kernarg_preload_length 0
		.amdhsa_user_sgpr_kernarg_preload_offset 0
		.amdhsa_user_sgpr_private_segment_size 0
		.amdhsa_uses_dynamic_stack 0
		.amdhsa_enable_private_segment 0
		.amdhsa_system_sgpr_workgroup_id_x 1
		.amdhsa_system_sgpr_workgroup_id_y 0
		.amdhsa_system_sgpr_workgroup_id_z 0
		.amdhsa_system_sgpr_workgroup_info 0
		.amdhsa_system_vgpr_workitem_id 0
		.amdhsa_next_free_vgpr 256
		.amdhsa_next_free_sgpr 102
		.amdhsa_accum_offset 256
		.amdhsa_reserve_vcc 1
		.amdhsa_float_round_mode_32 0
		.amdhsa_float_round_mode_16_64 0
		.amdhsa_float_denorm_mode_32 3
		.amdhsa_float_denorm_mode_16_64 3
		.amdhsa_dx10_clamp 1
		.amdhsa_ieee_mode 1
		.amdhsa_fp16_overflow 0
		.amdhsa_tg_split 0
		.amdhsa_exception_fp_ieee_invalid_op 0
		.amdhsa_exception_fp_denorm_src 0
		.amdhsa_exception_fp_ieee_div_zero 0
		.amdhsa_exception_fp_ieee_overflow 0
		.amdhsa_exception_fp_ieee_underflow 0
		.amdhsa_exception_fp_ieee_inexact 0
		.amdhsa_exception_int_div_zero 0
	.end_amdhsa_kernel

amdhsa.kernels:
  - .agpr_count:     0
    .args:
      - .offset:         0
        .size:           272
        .value_kind:     by_value
      - .offset:         272
        .size:           4
        .value_kind:     hidden_block_count_x
      - .offset:         276
        .size:           4
        .value_kind:     hidden_block_count_y
      - .offset:         280
        .size:           4
        .value_kind:     hidden_block_count_z
      - .offset:         284
        .size:           2
        .value_kind:     hidden_group_size_x
      - .offset:         286
        .size:           2
        .value_kind:     hidden_group_size_y
      - .offset:         288
        .size:           2
        .value_kind:     hidden_group_size_z
      - .offset:         290
        .size:           2
        .value_kind:     hidden_remainder_x
      - .offset:         292
        .size:           2
        .value_kind:     hidden_remainder_y
      - .offset:         294
        .size:           2
        .value_kind:     hidden_remainder_z
      - .offset:         312
        .size:           8
        .value_kind:     hidden_global_offset_x
      - .offset:         320
        .size:           8
        .value_kind:     hidden_global_offset_y
      - .offset:         328
        .size:           8
        .value_kind:     hidden_global_offset_z
      - .offset:         336
        .size:           2
        .value_kind:     hidden_grid_dims
      - .offset:         392
        .size:           4
        .value_kind:     hidden_dynamic_lds_size
    .group_segment_fixed_size: 0
    .kernarg_segment_align: 8
    .kernarg_segment_size: 528
    .language:       OpenCL C
    .language_version:
      - 2
      - 0
    .max_flat_workgroup_size: 512
    .name:           _Z10fwd_kernel6Params
    .private_segment_fixed_size: 0
    .sgpr_count:     108
    .sgpr_spill_count: 12
    .symbol:         _Z10fwd_kernel6Params.kd
    .uniform_work_group_size: 1
    .uses_dynamic_stack: false
    .vgpr_count:     256
    .vgpr_spill_count: 0
    .wavefront_size: 64
